# speedup vs baseline: 1.0428x; 1.0360x over previous
.Lno_anc:
	s_or_b64 exec, exec, s[8:9]
	v_mov_b32_e32 v7, 0x80
	s_waitcnt vmcnt(0)
	s_sub_u32 s26, 0x1ff, s2
	s_lshr_b32 s26, s26, 3
	s_cmp_eq_u32 s26, 0
	s_cbranch_scc1 .Lhold_done
